# expert-weight conversion loop: counted waits no longer drain the previous tile's stores (vmcnt 20 / 4), same split as the previous best (112 converter workgroups, 64 tiles in phase 1)
# speedup vs baseline: 1.0214x; 1.0050x over previous
.LBB0_366:
.LBB0_367:
	v_and_b32_e32 v66, 0x700, v200
	v_lshlrev_b32_e32 v66, 2, v66
	v_add3_u32 v142, 0, v66, v136
	v_and_b32_e32 v66, 0xff, v0
	v_lshrrev_b32_e32 v67, 8, v0
	v_or_b32_e32 v73, 0x200, v0
	v_or_b32_e32 v76, 0x600, v0
	v_lshlrev_b32_e32 v68, 16, v67
	v_lshlrev_b32_e32 v69, 2, v66
	v_lshrrev_b32_e32 v152, 3, v73
	v_lshrrev_b32_e32 v154, 3, v76
	v_add3_u32 v151, 0, v68, v69
	v_lshlrev_b32_e32 v67, 2, v67
	v_and_b32_e32 v68, 7, v0
	v_xor_b32_e32 v72, v140, v0
	v_xor_b32_e32 v74, v152, v0
	v_xor_b32_e32 v77, v154, v0
	v_bitop3_b32 v69, v67, v0, 7 bitop3:0x78
	v_bitop3_b32 v70, v67, v68, 1 bitop3:0x36
	v_bitop3_b32 v71, v67, v68, 2 bitop3:0x36
	v_bitop3_b32 v67, v67, v68, 3 bitop3:0x36
	v_lshlrev_b32_e32 v72, 4, v72
	v_lshlrev_b32_e32 v74, 4, v74
	v_or_b32_e32 v153, 0x80, v140
	v_lshlrev_b32_e32 v77, 4, v77
	v_lshl_add_u32 v66, v66, 7, 0
	v_lshlrev_b32_e32 v69, 4, v69
	v_lshlrev_b32_e32 v70, 4, v70
	v_lshlrev_b32_e32 v71, 4, v71
	v_lshlrev_b32_e32 v67, 4, v67
	v_lshlrev_b32_e32 v138, 4, v68
	v_lshl_add_u32 v68, v140, 7, 0
	v_and_b32_e32 v72, 0x70, v72
	v_lshl_add_u32 v73, v152, 7, 0
	v_and_b32_e32 v74, 0x70, v74
	v_lshl_add_u32 v75, v153, 7, 0
	v_lshl_add_u32 v76, v154, 7, 0
	v_and_b32_e32 v77, 0x70, v77
	s_mov_b32 s9, 0
	v_add_u32_e32 v143, 0x10000, v142
	v_add_u32_e32 v144, 0x12000, v142
	v_add_u32_e32 v145, 0x14000, v142
	v_add_u32_e32 v146, 0x16000, v142
	v_add_u32_e32 v147, 0x18000, v142
	v_add_u32_e32 v148, 0x1a000, v142
	v_add_u32_e32 v149, 0x1c000, v142
	v_add_u32_e32 v150, 0x1e000, v142
	v_mov_b32_e32 v139, v135
	s_mov_b32 s11, 0xc3e00000
	s_movk_i32 s16, 0x3c0
	v_mov_b32_e32 v155, 0x43e00000
	v_add_u32_e32 v156, v66, v69
	v_add_u32_e32 v157, v66, v70
	v_add_u32_e32 v158, v66, v71
	v_add_u32_e32 v159, v66, v67
	v_add_u32_e32 v160, v68, v72
	v_add_u32_e32 v161, v73, v74
	v_add_u32_e32 v162, v75, v72
	v_add_u32_e32 v163, v76, v77
	s_mov_b32 s18, s12
	s_waitcnt vmcnt(0)
	s_branch .LBB0_370

.LBB0_377:
	v_mul_u32_u24_e32 v66, s46, v141
	v_lshlrev_b32_e32 v134, 2, v66
	v_lshl_add_u64 v[66:67], s[2:3], 0, v[134:135]
	v_mov_b32_e32 v137, v135
	v_lshl_add_u64 v[66:67], v[66:67], 0, v[136:137]
	s_lshl_b32 s8, s46, 5
	v_lshl_add_u64 v[74:75], v[66:67], 0, s[8:9]
	global_load_dwordx4 v[66:69], v[66:67], off nt
	s_nop 0
	global_load_dwordx4 v[70:73], v[74:75], off nt
	v_lshl_add_u64 v[74:75], v[74:75], 0, s[8:9]
	v_lshl_add_u64 v[82:83], v[74:75], 0, s[8:9]
	global_load_dwordx4 v[74:77], v[74:75], off nt
	s_nop 0
	global_load_dwordx4 v[78:81], v[82:83], off nt
	v_lshl_add_u64 v[82:83], v[82:83], 0, s[8:9]
	v_lshl_add_u64 v[90:91], v[82:83], 0, s[8:9]
	global_load_dwordx4 v[82:85], v[82:83], off nt
	s_nop 0
	global_load_dwordx4 v[86:89], v[90:91], off nt
	v_lshl_add_u64 v[90:91], v[90:91], 0, s[8:9]
	v_lshl_add_u64 v[98:99], v[90:91], 0, s[8:9]
	v_lshl_add_u64 v[102:103], v[98:99], 0, s[8:9]
	v_lshl_add_u64 v[106:107], v[102:103], 0, s[8:9]
	v_lshl_add_u64 v[110:111], v[106:107], 0, s[8:9]
	v_lshl_add_u64 v[114:115], v[110:111], 0, s[8:9]
	v_lshl_add_u64 v[118:119], v[114:115], 0, s[8:9]
	v_lshl_add_u64 v[122:123], v[118:119], 0, s[8:9]
	v_lshl_add_u64 v[126:127], v[122:123], 0, s[8:9]
	global_load_dwordx4 v[90:93], v[90:91], off nt
	s_nop 0
	global_load_dwordx4 v[94:97], v[98:99], off nt
	s_nop 0
	global_load_dwordx4 v[98:101], v[102:103], off nt
	s_nop 0
	global_load_dwordx4 v[102:105], v[106:107], off nt
	s_nop 0
	global_load_dwordx4 v[106:109], v[110:111], off nt
	s_nop 0
	global_load_dwordx4 v[110:113], v[114:115], off nt
	s_nop 0
	global_load_dwordx4 v[114:117], v[118:119], off nt
	s_nop 0
	global_load_dwordx4 v[118:121], v[122:123], off nt
	s_nop 0
	global_load_dwordx4 v[122:125], v[126:127], off nt
	v_lshl_add_u64 v[126:127], v[126:127], 0, s[8:9]
	global_load_dwordx4 v[126:129], v[126:127], off nt
	s_waitcnt vmcnt(20)
	s_branch .Lmoe_w1
.LBB0_378:
	s_waitcnt vmcnt(4)

.LBB0_401:
	v_mul_u32_u24_e32 v2, s44, v141
	v_lshlrev_b32_e32 v134, 2, v2
	v_lshl_add_u64 v[2:3], s[2:3], 0, v[134:135]
	v_mov_b32_e32 v137, v135
	v_lshl_add_u64 v[2:3], v[2:3], 0, v[136:137]
	s_lshl_b32 s8, s44, 5
	v_lshl_add_u64 v[10:11], v[2:3], 0, s[8:9]
	global_load_dwordx4 v[2:5], v[2:3], off nt
	s_nop 0
	global_load_dwordx4 v[6:9], v[10:11], off nt
	v_lshl_add_u64 v[10:11], v[10:11], 0, s[8:9]
	v_lshl_add_u64 v[18:19], v[10:11], 0, s[8:9]
	global_load_dwordx4 v[10:13], v[10:11], off nt
	s_nop 0
	global_load_dwordx4 v[14:17], v[18:19], off nt
	v_lshl_add_u64 v[18:19], v[18:19], 0, s[8:9]
	v_lshl_add_u64 v[26:27], v[18:19], 0, s[8:9]
	global_load_dwordx4 v[18:21], v[18:19], off nt
	s_nop 0
	global_load_dwordx4 v[22:25], v[26:27], off nt
	v_lshl_add_u64 v[26:27], v[26:27], 0, s[8:9]
	v_lshl_add_u64 v[34:35], v[26:27], 0, s[8:9]
	v_lshl_add_u64 v[38:39], v[34:35], 0, s[8:9]
	v_lshl_add_u64 v[42:43], v[38:39], 0, s[8:9]
	v_lshl_add_u64 v[46:47], v[42:43], 0, s[8:9]
	v_lshl_add_u64 v[50:51], v[46:47], 0, s[8:9]
	v_lshl_add_u64 v[54:55], v[50:51], 0, s[8:9]
	v_lshl_add_u64 v[58:59], v[54:55], 0, s[8:9]
	v_lshl_add_u64 v[62:63], v[58:59], 0, s[8:9]
	global_load_dwordx4 v[26:29], v[26:27], off nt
	s_nop 0
	global_load_dwordx4 v[30:33], v[34:35], off nt
	s_nop 0
	global_load_dwordx4 v[34:37], v[38:39], off nt
	s_nop 0
	global_load_dwordx4 v[38:41], v[42:43], off nt
	s_nop 0
	global_load_dwordx4 v[42:45], v[46:47], off nt
	s_nop 0
	global_load_dwordx4 v[46:49], v[50:51], off nt
	s_nop 0
	global_load_dwordx4 v[50:53], v[54:55], off nt
	s_nop 0
	global_load_dwordx4 v[54:57], v[58:59], off nt
	s_nop 0
	global_load_dwordx4 v[58:61], v[62:63], off nt
	v_lshl_add_u64 v[62:63], v[62:63], 0, s[8:9]
	global_load_dwordx4 v[62:65], v[62:63], off nt
	s_waitcnt vmcnt(20)
	s_branch .Lmoe_w2

.Lcv_366:
.Lcv_367:
	v_and_b32_e32 v66, 0x700, v200
	v_lshlrev_b32_e32 v66, 2, v66
	v_add3_u32 v142, 0, v66, v136
	v_and_b32_e32 v66, 0xff, v0
	v_lshrrev_b32_e32 v67, 8, v0
	v_or_b32_e32 v73, 0x200, v0
	v_or_b32_e32 v76, 0x600, v0
	v_lshlrev_b32_e32 v68, 16, v67
	v_lshlrev_b32_e32 v69, 2, v66
	v_lshrrev_b32_e32 v152, 3, v73
	v_lshrrev_b32_e32 v154, 3, v76
	v_add3_u32 v151, 0, v68, v69
	v_lshlrev_b32_e32 v67, 2, v67
	v_and_b32_e32 v68, 7, v0
	v_xor_b32_e32 v72, v140, v0
	v_xor_b32_e32 v74, v152, v0
	v_xor_b32_e32 v77, v154, v0
	v_bitop3_b32 v69, v67, v0, 7 bitop3:0x78
	v_bitop3_b32 v70, v67, v68, 1 bitop3:0x36
	v_bitop3_b32 v71, v67, v68, 2 bitop3:0x36
	v_bitop3_b32 v67, v67, v68, 3 bitop3:0x36
	v_lshlrev_b32_e32 v72, 4, v72
	v_lshlrev_b32_e32 v74, 4, v74
	v_or_b32_e32 v153, 0x80, v140
	v_lshlrev_b32_e32 v77, 4, v77
	v_lshl_add_u32 v66, v66, 7, 0
	v_lshlrev_b32_e32 v69, 4, v69
	v_lshlrev_b32_e32 v70, 4, v70
	v_lshlrev_b32_e32 v71, 4, v71
	v_lshlrev_b32_e32 v67, 4, v67
	v_lshlrev_b32_e32 v138, 4, v68
	v_lshl_add_u32 v68, v140, 7, 0
	v_and_b32_e32 v72, 0x70, v72
	v_lshl_add_u32 v73, v152, 7, 0
	v_and_b32_e32 v74, 0x70, v74
	v_lshl_add_u32 v75, v153, 7, 0
	v_lshl_add_u32 v76, v154, 7, 0
	v_and_b32_e32 v77, 0x70, v77
	s_mov_b32 s9, 0
	v_add_u32_e32 v143, 0x10000, v142
	v_add_u32_e32 v144, 0x12000, v142
	v_add_u32_e32 v145, 0x14000, v142
	v_add_u32_e32 v146, 0x16000, v142
	v_add_u32_e32 v147, 0x18000, v142
	v_add_u32_e32 v148, 0x1a000, v142
	v_add_u32_e32 v149, 0x1c000, v142
	v_add_u32_e32 v150, 0x1e000, v142
	v_mov_b32_e32 v139, v135
	s_mov_b32 s11, 0xc3e00000
	s_movk_i32 s68, 0x3c0
	v_mov_b32_e32 v155, 0x43e00000
	v_add_u32_e32 v156, v66, v69
	v_add_u32_e32 v157, v66, v70
	v_add_u32_e32 v158, v66, v71
	v_add_u32_e32 v159, v66, v67
	v_add_u32_e32 v160, v68, v72
	v_add_u32_e32 v161, v73, v74
	v_add_u32_e32 v162, v75, v72
	v_add_u32_e32 v163, v76, v77
	s_mov_b32 s18, s12
	s_waitcnt vmcnt(0)
	s_branch .Lcv_370
